# grid barrier followers poll the global generation word directly; out-projection gated-residual epilogues keep 2-3 row groups of residual loads in flight (both layers)
# speedup vs baseline: 1.0253x; 1.0053x over previous
; __device__ __forceinline__ unsigned xb_ld(unsigned* p)              { return __hip_atomic_load(p, __ATOMIC_RELAXED, __HIP_MEMORY_SCOPE_AGENT); }
; __device__ __forceinline__ unsigned xb_add(unsigned* p, unsigned v) { return __hip_atomic_fetch_add(p, v, __ATOMIC_RELAXED, __HIP_MEMORY_SCOPE_AGENT); }
; #define XB_SPIN(cond, bar) do { unsigned _sp = 0; while (cond) { __builtin_amdgcn_s_sleep(1); \
;     if ((++_sp & 255u) == 0u) { if (xb_ld(&(bar)[XB_TMO])) break; if (_sp > XB_SPIN_CAP) { atomicAdd(&(bar)[XB_TMO], 1u); break; } } } } while (0)
; __device__ __forceinline__ void xcd_barrier(const XcdBarrier& b) {
;     ...
;         if (nloc == 0u) { xcd_barrier_complete(bar, b.x, nloc, nx); b.st[0] = nloc; b.st[1] = nx; }
;         const unsigned old = xb_add(&bar[XB_XSUB(b.x)], 1u);
;         const unsigned gen = old / nloc;
;         if (old + 1u == (gen + 1u) * nloc) {
;             __builtin_amdgcn_fence(__ATOMIC_RELEASE, "agent");
;             asm volatile("s_waitcnt vmcnt(0)" ::: "memory");
;             const unsigned og = xb_add(&bar[XB_TOP], 1u);
;             const unsigned tg = og / nx;
;             if (og + 1u == (tg + 1u) * nx) xb_add(&bar[XB_TOPGEN], 1u);
;             else XB_SPIN(xb_ld(&bar[XB_TOPGEN]) == tg, bar);
;             __builtin_amdgcn_fence(__ATOMIC_ACQUIRE, "agent");
;             xb_add(&bar[XB_XGEN(b.x)], 1u);
;             asm volatile("s_waitcnt vmcnt(0)" ::: "memory");
;         } else {
;             XB_SPIN(xb_ld(&bar[XB_XGEN(b.x)]) == gen, bar);
.LBB0_182:
	s_lshl_b32 s4, s92, 8
	v_readlane_b32 s6, v255, 8
	v_readlane_b32 s7, v255, 9
	s_add_u32 s4, s6, s4
	s_addc_u32 s5, s7, 0
	v_mov_b32_e32 v2, 0x1000
	v_mov_b32_e32 v4, 1
	global_atomic_add v4, v2, v4, s[4:5] offset:1024 sc0
	v_cvt_f32_u32_e32 v2, v3
	v_sub_u32_e32 v5, 0, v3
	v_rcp_iflag_f32_e32 v2, v2
	s_nop 0
	v_mul_f32_e32 v2, 0x4f7ffffe, v2
	v_cvt_u32_f32_e32 v2, v2
	v_mul_lo_u32 v5, v5, v2
	v_mul_hi_u32 v5, v2, v5
	v_add_u32_e32 v2, v2, v5
	s_waitcnt vmcnt(0)
	v_mul_hi_u32 v2, v4, v2
	v_mul_lo_u32 v5, v2, v3
	v_sub_u32_e32 v5, v4, v5
	v_add_u32_e32 v6, 1, v2
	v_cmp_ge_u32_e32 vcc, v5, v3
	v_add_u32_e32 v4, 1, v4
	s_nop 0
	v_cndmask_b32_e32 v2, v2, v6, vcc
	v_sub_u32_e32 v6, v5, v3
	v_cndmask_b32_e32 v5, v5, v6, vcc
	v_add_u32_e32 v6, 1, v2
	v_cmp_ge_u32_e32 vcc, v5, v3
	s_nop 1
	v_cndmask_b32_e32 v2, v2, v6, vcc
	v_mul_lo_u32 v5, v3, v2
	v_add_u32_e32 v3, v5, v3
	v_cmp_ne_u32_e32 vcc, v4, v3
	s_and_saveexec_b64 s[6:7], vcc
	s_xor_b64 s[6:7], exec, s[6:7]
	s_cbranch_execz .LBB0_196
	s_waitcnt lgkmcnt(0)
	v_readlane_b32 s10, v255, 8
	v_readlane_b32 s11, v255, 9
	v_mov_b32_e32 v1, 0
	s_nop 3
	s_add_u32 s10, s10, 0x3500
	s_addc_u32 s11, s11, 0
	global_load_dword v1, v1, s[10:11] sc1
	s_waitcnt vmcnt(0)
	v_cmp_eq_u32_e32 vcc, v1, v2
	s_and_saveexec_b64 s[8:9], vcc
	s_cbranch_execz .LBB0_195
	s_mov_b32 s24, 1
	s_mov_b64 s[12:13], 0
	v_mov_b32_e32 v1, 0
	s_branch .LBB0_186

; __device__ __forceinline__ unsigned xb_ld(unsigned* p)              { return __hip_atomic_load(p, __ATOMIC_RELAXED, __HIP_MEMORY_SCOPE_AGENT); }
; __device__ __forceinline__ unsigned xb_add(unsigned* p, unsigned v) { return __hip_atomic_fetch_add(p, v, __ATOMIC_RELAXED, __HIP_MEMORY_SCOPE_AGENT); }
; #define XB_SPIN(cond, bar) do { unsigned _sp = 0; while (cond) { __builtin_amdgcn_s_sleep(1); \
;     if ((++_sp & 255u) == 0u) { if (xb_ld(&(bar)[XB_TMO])) break; if (_sp > XB_SPIN_CAP) { atomicAdd(&(bar)[XB_TMO], 1u); break; } } } } while (0)
; __device__ __forceinline__ void xcd_barrier(const XcdBarrier& b) {
;     ...
;             const unsigned og = xb_add(&bar[XB_TOP], 1u);
;             const unsigned tg = og / nx;
;             if (og + 1u == (tg + 1u) * nx) xb_add(&bar[XB_TOPGEN], 1u);
;             else XB_SPIN(xb_ld(&bar[XB_TOPGEN]) == tg, bar);
;             __builtin_amdgcn_fence(__ATOMIC_ACQUIRE, "agent");
;             xb_add(&bar[XB_XGEN(b.x)], 1u);
;             asm volatile("s_waitcnt vmcnt(0)" ::: "memory");
.LBB0_213:
	s_or_b64 exec, exec, s[6:7]
	v_mov_b32_e32 v1, 0x2000
	v_mov_b32_e32 v2, 1
	s_waitcnt vmcnt(0)
	buffer_inv sc1
	s_waitcnt vmcnt(0)

; __device__ __forceinline__ unsigned cvt_pk_bf16(float lo, float hi) { unsigned r; asm volatile("v_cvt_pk_bf16_f32 %0, %1, %2" : "=v"(r) : "v"(lo), "v"(hi)); return r; }
; __device__ __forceinline__ float bf_lo(unsigned w) { return __uint_as_float(w << 16); }
; __device__ __forceinline__ float bf_hi(unsigned w) { return __uint_as_float(w & 0xffff0000u); }
;     __device__ __forceinline__ void operator()(const f32x4 (&acc)[2][2][4][2], const Unit& u, int wr, int wc, int fr, int fq) const {
;         const int row0 = u.pm * BM + wr * 64 + fr, col0 = u.pn * BM + wc * 64 + 16 * fq;
;         const float* gp = gate + (size_t)((u.pm * BM) / S) * MODW + col0;
;         f32x4 gv[4];
; #pragma unroll
;         for (int q = 0; q < 4; ++q) gv[q] = *(const f32x4*)(gp + 4 * q) * sc;
; #pragma unroll
;         for (int ai = 0; ai < 2; ++ai)
; #pragma unroll
;             for (int m = 0; m < 4; ++m) { const size_t off = (size_t)(row0 + ai * HALF + m * 16) * D + col0; f32x4 r[4];
;                 if (RBF) { const u32x4 w0 = *(const u32x4*)((const bf16_t*)R + off), w1 = *(const u32x4*)((const bf16_t*)R + off + 8);
;                     r[0] = (f32x4){bf_lo(w0.x), bf_hi(w0.x), bf_lo(w0.y), bf_hi(w0.y)}; r[1] = (f32x4){bf_lo(w0.z), bf_hi(w0.z), bf_lo(w0.w), bf_hi(w0.w)};
;                     r[2] = (f32x4){bf_lo(w1.x), bf_hi(w1.x), bf_lo(w1.y), bf_hi(w1.y)}; r[3] = (f32x4){bf_lo(w1.z), bf_hi(w1.z), bf_lo(w1.w), bf_hi(w1.w)}; }
;                 else {
; #pragma unroll
;                     for (int q = 0; q < 4; ++q) r[q] = *(const f32x4*)((const float*)R + off + 4 * q); }
; #pragma unroll
;                 for (int q = 0; q < 4; ++q) r[q] = r[q] + gv[q] * acc[ai][q >> 1][m][q & 1];
;                 u32x4 o0, o1; o0.x = cvt_pk_bf16(r[0][0], r[0][1]); o0.y = cvt_pk_bf16(r[0][2], r[0][3]); o0.z = cvt_pk_bf16(r[1][0], r[1][1]); o0.w = cvt_pk_bf16(r[1][2], r[1][3]);
;                 o1.x = cvt_pk_bf16(r[2][0], r[2][1]); o1.y = cvt_pk_bf16(r[2][2], r[2][3]); o1.z = cvt_pk_bf16(r[3][0], r[3][1]); o1.w = cvt_pk_bf16(r[3][2], r[3][3]);
;                 *(u32x4*)(out + off) = o0; *(u32x4*)(out + off + 8) = o1; }
.LBB0_463:
	s_ashr_i32 s24, s62, 31
	s_lshr_b32 s24, s24, 28
	s_add_i32 s24, s62, s24
	s_ashr_i32 s24, s24, 4
	s_mul_hi_i32 s25, s24, 0xc000
	s_mul_i32 s24, s24, 0xc000
	v_lshl_or_b32 v20, s63, 8, v243
	s_add_u32 s24, s47, s24
	s_addc_u32 s25, s48, s25
	v_ashrrev_i32_e32 v21, 31, v20
	v_lshl_add_u32 v22, s62, 8, v1
	s_nop 15
	s_nop 7
	v_lshlrev_b32_e32 v60, 2, v20
	v_lshlrev_b32_e32 v62, 11, v22
	global_load_dwordx4 v[4:7], v60, s[24:25]
	global_load_dwordx4 v[8:11], v60, s[24:25] offset:16
	global_load_dwordx4 v[12:15], v60, s[24:25] offset:32
	global_load_dwordx4 v[16:19], v60, s[24:25] offset:48
	v_add_u32_e32 v62, v62, v20
	v_lshlrev_b32_e32 v63, 1, v62
	v_lshlrev_b32_e32 v62, 2, v62
	global_load_dwordx4 v[24:27], v62, s[18:19]
	global_load_dwordx4 v[28:31], v62, s[18:19] offset:16
	global_load_dwordx4 v[32:35], v62, s[18:19] offset:32
	global_load_dwordx4 v[36:39], v62, s[18:19] offset:48
	v_add_u32_e32 v62, 0x20000, v62
	global_load_dwordx4 v[40:43], v62, s[18:19]
	global_load_dwordx4 v[44:47], v62, s[18:19] offset:16
	global_load_dwordx4 v[48:51], v62, s[18:19] offset:32
	global_load_dwordx4 v[52:55], v62, s[18:19] offset:48
	s_and_b64 vcc, exec, s[6:7]
	s_mov_b64 s[6:7], -1
	s_waitcnt vmcnt(8)
	v_pk_mul_f32 v[4:5], v[4:5], s[20:21] op_sel_hi:[1,0]
	v_pk_mul_f32 v[6:7], v[6:7], s[20:21] op_sel_hi:[1,0]
	v_pk_mul_f32 v[8:9], v[8:9], s[20:21] op_sel_hi:[1,0]
	v_pk_mul_f32 v[10:11], v[10:11], s[20:21] op_sel_hi:[1,0]
	v_pk_mul_f32 v[12:13], v[12:13], s[20:21] op_sel_hi:[1,0]
	v_pk_mul_f32 v[14:15], v[14:15], s[20:21] op_sel_hi:[1,0]
	v_pk_mul_f32 v[16:17], v[16:17], s[20:21] op_sel_hi:[1,0]
	v_pk_mul_f32 v[18:19], v[18:19], s[20:21] op_sel_hi:[1,0]
	s_waitcnt vmcnt(4)
	v_pk_fma_f32 v[24:25], v[190:191], v[4:5], v[24:25]
	v_pk_fma_f32 v[26:27], v[192:193], v[6:7], v[26:27]
	v_pk_fma_f32 v[28:29], v[186:187], v[8:9], v[28:29]
	v_pk_fma_f32 v[30:31], v[188:189], v[10:11], v[30:31]
	v_pk_fma_f32 v[32:33], v[182:183], v[12:13], v[32:33]
	v_pk_fma_f32 v[34:35], v[184:185], v[14:15], v[34:35]
	v_pk_fma_f32 v[36:37], v[178:179], v[16:17], v[36:37]
	v_pk_fma_f32 v[38:39], v[180:181], v[18:19], v[38:39]
	v_cvt_pk_bf16_f32 v24, v24, v25
	v_cvt_pk_bf16_f32 v25, v26, v27
	v_cvt_pk_bf16_f32 v26, v28, v29
	v_cvt_pk_bf16_f32 v27, v30, v31
	v_cvt_pk_bf16_f32 v28, v32, v33
	v_cvt_pk_bf16_f32 v29, v34, v35
	v_cvt_pk_bf16_f32 v30, v36, v37
	v_cvt_pk_bf16_f32 v31, v38, v39
	s_nop 0
	global_store_dwordx4 v63, v[24:27], s[72:73]
	global_store_dwordx4 v63, v[28:31], s[72:73] offset:16
	v_add_u32_e32 v63, 0x10000, v63
	v_add_u32_e32 v62, 0x20000, v62
	global_load_dwordx4 v[24:27], v62, s[18:19]
	global_load_dwordx4 v[28:31], v62, s[18:19] offset:16
	global_load_dwordx4 v[32:35], v62, s[18:19] offset:32
	global_load_dwordx4 v[36:39], v62, s[18:19] offset:48
	s_waitcnt vmcnt(6)
	v_pk_fma_f32 v[40:41], v[174:175], v[4:5], v[40:41]
	v_pk_fma_f32 v[42:43], v[176:177], v[6:7], v[42:43]
	v_pk_fma_f32 v[44:45], v[170:171], v[8:9], v[44:45]
	v_pk_fma_f32 v[46:47], v[172:173], v[10:11], v[46:47]
	v_pk_fma_f32 v[48:49], v[166:167], v[12:13], v[48:49]
	v_pk_fma_f32 v[50:51], v[168:169], v[14:15], v[50:51]
	v_pk_fma_f32 v[52:53], v[162:163], v[16:17], v[52:53]
	v_pk_fma_f32 v[54:55], v[164:165], v[18:19], v[54:55]
	v_cvt_pk_bf16_f32 v40, v40, v41
	v_cvt_pk_bf16_f32 v41, v42, v43
	v_cvt_pk_bf16_f32 v42, v44, v45
	v_cvt_pk_bf16_f32 v43, v46, v47
	v_cvt_pk_bf16_f32 v44, v48, v49
	v_cvt_pk_bf16_f32 v45, v50, v51
	v_cvt_pk_bf16_f32 v46, v52, v53
	v_cvt_pk_bf16_f32 v47, v54, v55
	s_nop 0
	global_store_dwordx4 v63, v[40:43], s[72:73]
	global_store_dwordx4 v63, v[44:47], s[72:73] offset:16
	v_add_u32_e32 v63, 0x10000, v63
	v_add_u32_e32 v62, 0x20000, v62
	global_load_dwordx4 v[40:43], v62, s[18:19]
	global_load_dwordx4 v[44:47], v62, s[18:19] offset:16
	global_load_dwordx4 v[48:51], v62, s[18:19] offset:32
	global_load_dwordx4 v[52:55], v62, s[18:19] offset:48
	s_waitcnt vmcnt(6)
	v_pk_fma_f32 v[24:25], v[158:159], v[4:5], v[24:25]
	v_pk_fma_f32 v[26:27], v[160:161], v[6:7], v[26:27]
	v_pk_fma_f32 v[28:29], v[154:155], v[8:9], v[28:29]
	v_pk_fma_f32 v[30:31], v[156:157], v[10:11], v[30:31]
	v_pk_fma_f32 v[32:33], v[150:151], v[12:13], v[32:33]
	v_pk_fma_f32 v[34:35], v[152:153], v[14:15], v[34:35]
	v_pk_fma_f32 v[36:37], v[146:147], v[16:17], v[36:37]
	v_pk_fma_f32 v[38:39], v[148:149], v[18:19], v[38:39]
	v_cvt_pk_bf16_f32 v24, v24, v25
	v_cvt_pk_bf16_f32 v25, v26, v27
	v_cvt_pk_bf16_f32 v26, v28, v29
	v_cvt_pk_bf16_f32 v27, v30, v31
	v_cvt_pk_bf16_f32 v28, v32, v33
	v_cvt_pk_bf16_f32 v29, v34, v35
	v_cvt_pk_bf16_f32 v30, v36, v37
	v_cvt_pk_bf16_f32 v31, v38, v39
	s_nop 0
	global_store_dwordx4 v63, v[24:27], s[72:73]
	global_store_dwordx4 v63, v[28:31], s[72:73] offset:16
	v_add_u32_e32 v63, 0x10000, v63
	v_add_u32_e32 v62, 0xa0000, v62
	global_load_dwordx4 v[24:27], v62, s[18:19]
	global_load_dwordx4 v[28:31], v62, s[18:19] offset:16
	global_load_dwordx4 v[32:35], v62, s[18:19] offset:32
	global_load_dwordx4 v[36:39], v62, s[18:19] offset:48
	s_waitcnt vmcnt(6)
; __device__ __forceinline__ unsigned cvt_pk_bf16(float lo, float hi) { unsigned r; asm volatile("v_cvt_pk_bf16_f32 %0, %1, %2" : "=v"(r) : "v"(lo), "v"(hi)); return r; }
; __device__ __forceinline__ float bf_lo(unsigned w) { return __uint_as_float(w << 16); }
; __device__ __forceinline__ float bf_hi(unsigned w) { return __uint_as_float(w & 0xffff0000u); }
;     __device__ __forceinline__ void operator()(const f32x4 (&acc)[2][2][4][2], const Unit& u, int wr, int wc, int fr, int fq) const {
;     ...
;         for (int ai = 0; ai < 2; ++ai)
; #pragma unroll
;             for (int m = 0; m < 4; ++m) { const size_t off = (size_t)(row0 + ai * HALF + m * 16) * D + col0; f32x4 r[4];
;                 if (RBF) { const u32x4 w0 = *(const u32x4*)((const bf16_t*)R + off), w1 = *(const u32x4*)((const bf16_t*)R + off + 8);
;                     r[0] = (f32x4){bf_lo(w0.x), bf_hi(w0.x), bf_lo(w0.y), bf_hi(w0.y)}; r[1] = (f32x4){bf_lo(w0.z), bf_hi(w0.z), bf_lo(w0.w), bf_hi(w0.w)};
;                     r[2] = (f32x4){bf_lo(w1.x), bf_hi(w1.x), bf_lo(w1.y), bf_hi(w1.y)}; r[3] = (f32x4){bf_lo(w1.z), bf_hi(w1.z), bf_lo(w1.w), bf_hi(w1.w)}; }
;                 else {
; #pragma unroll
;                     for (int q = 0; q < 4; ++q) r[q] = *(const f32x4*)((const float*)R + off + 4 * q); }
; #pragma unroll
;                 for (int q = 0; q < 4; ++q) r[q] = r[q] + gv[q] * acc[ai][q >> 1][m][q & 1];
;                 u32x4 o0, o1; o0.x = cvt_pk_bf16(r[0][0], r[0][1]); o0.y = cvt_pk_bf16(r[0][2], r[0][3]); o0.z = cvt_pk_bf16(r[1][0], r[1][1]); o0.w = cvt_pk_bf16(r[1][2], r[1][3]);
;                 o1.x = cvt_pk_bf16(r[2][0], r[2][1]); o1.y = cvt_pk_bf16(r[2][2], r[2][3]); o1.z = cvt_pk_bf16(r[3][0], r[3][1]); o1.w = cvt_pk_bf16(r[3][2], r[3][3]);
;                 *(u32x4*)(out + off) = o0; *(u32x4*)(out + off + 8) = o1; }
	v_pk_fma_f32 v[40:41], v[142:143], v[4:5], v[40:41]
	v_pk_fma_f32 v[42:43], v[144:145], v[6:7], v[42:43]
	v_pk_fma_f32 v[44:45], v[138:139], v[8:9], v[44:45]
	v_pk_fma_f32 v[46:47], v[140:141], v[10:11], v[46:47]
	v_pk_fma_f32 v[48:49], v[134:135], v[12:13], v[48:49]
	v_pk_fma_f32 v[50:51], v[136:137], v[14:15], v[50:51]
	v_pk_fma_f32 v[52:53], v[130:131], v[16:17], v[52:53]
	v_pk_fma_f32 v[54:55], v[132:133], v[18:19], v[54:55]
	v_cvt_pk_bf16_f32 v40, v40, v41
	v_cvt_pk_bf16_f32 v41, v42, v43
	v_cvt_pk_bf16_f32 v42, v44, v45
	v_cvt_pk_bf16_f32 v43, v46, v47
	v_cvt_pk_bf16_f32 v44, v48, v49
	v_cvt_pk_bf16_f32 v45, v50, v51
	v_cvt_pk_bf16_f32 v46, v52, v53
	v_cvt_pk_bf16_f32 v47, v54, v55
	s_nop 0
	global_store_dwordx4 v63, v[40:43], s[72:73]
	global_store_dwordx4 v63, v[44:47], s[72:73] offset:16
	v_add_u32_e32 v63, 0x50000, v63
	v_add_u32_e32 v62, 0x20000, v62
	global_load_dwordx4 v[40:43], v62, s[18:19]
	global_load_dwordx4 v[44:47], v62, s[18:19] offset:16
	global_load_dwordx4 v[48:51], v62, s[18:19] offset:32
	global_load_dwordx4 v[52:55], v62, s[18:19] offset:48
	s_waitcnt vmcnt(6)
	v_pk_fma_f32 v[24:25], v[126:127], v[4:5], v[24:25]
	v_pk_fma_f32 v[26:27], v[128:129], v[6:7], v[26:27]
	v_pk_fma_f32 v[28:29], v[122:123], v[8:9], v[28:29]
	v_pk_fma_f32 v[30:31], v[124:125], v[10:11], v[30:31]
	v_pk_fma_f32 v[32:33], v[118:119], v[12:13], v[32:33]
	v_pk_fma_f32 v[34:35], v[120:121], v[14:15], v[34:35]
	v_pk_fma_f32 v[36:37], v[114:115], v[16:17], v[36:37]
	v_pk_fma_f32 v[38:39], v[116:117], v[18:19], v[38:39]
	v_cvt_pk_bf16_f32 v24, v24, v25
	v_cvt_pk_bf16_f32 v25, v26, v27
	v_cvt_pk_bf16_f32 v26, v28, v29
	v_cvt_pk_bf16_f32 v27, v30, v31
	v_cvt_pk_bf16_f32 v28, v32, v33
	v_cvt_pk_bf16_f32 v29, v34, v35
	v_cvt_pk_bf16_f32 v30, v36, v37
	v_cvt_pk_bf16_f32 v31, v38, v39
	s_nop 0
	global_store_dwordx4 v63, v[24:27], s[72:73]
	global_store_dwordx4 v63, v[28:31], s[72:73] offset:16
	v_add_u32_e32 v63, 0x10000, v63
	v_add_u32_e32 v62, 0x20000, v62
	global_load_dwordx4 v[24:27], v62, s[18:19]
	global_load_dwordx4 v[28:31], v62, s[18:19] offset:16
	global_load_dwordx4 v[32:35], v62, s[18:19] offset:32
	global_load_dwordx4 v[36:39], v62, s[18:19] offset:48
	s_waitcnt vmcnt(6)
	v_pk_fma_f32 v[40:41], v[110:111], v[4:5], v[40:41]
	v_pk_fma_f32 v[42:43], v[112:113], v[6:7], v[42:43]
	v_pk_fma_f32 v[44:45], v[106:107], v[8:9], v[44:45]
	v_pk_fma_f32 v[46:47], v[108:109], v[10:11], v[46:47]
	v_pk_fma_f32 v[48:49], v[102:103], v[12:13], v[48:49]
	v_pk_fma_f32 v[50:51], v[104:105], v[14:15], v[50:51]
	v_pk_fma_f32 v[52:53], v[98:99], v[16:17], v[52:53]
	v_pk_fma_f32 v[54:55], v[100:101], v[18:19], v[54:55]
	v_cvt_pk_bf16_f32 v40, v40, v41
	v_cvt_pk_bf16_f32 v41, v42, v43
	v_cvt_pk_bf16_f32 v42, v44, v45
	v_cvt_pk_bf16_f32 v43, v46, v47
	v_cvt_pk_bf16_f32 v44, v48, v49
	v_cvt_pk_bf16_f32 v45, v50, v51
	v_cvt_pk_bf16_f32 v46, v52, v53
	v_cvt_pk_bf16_f32 v47, v54, v55
	s_nop 0
	global_store_dwordx4 v63, v[40:43], s[72:73]
	global_store_dwordx4 v63, v[44:47], s[72:73] offset:16
	v_add_u32_e32 v63, 0x10000, v63
	v_add_u32_e32 v62, 0x20000, v62
	global_load_dwordx4 v[40:43], v62, s[18:19]
	global_load_dwordx4 v[44:47], v62, s[18:19] offset:16
	global_load_dwordx4 v[48:51], v62, s[18:19] offset:32
	global_load_dwordx4 v[52:55], v62, s[18:19] offset:48
	s_waitcnt vmcnt(6)
	v_pk_fma_f32 v[24:25], v[94:95], v[4:5], v[24:25]
	v_pk_fma_f32 v[26:27], v[96:97], v[6:7], v[26:27]
	v_pk_fma_f32 v[28:29], v[90:91], v[8:9], v[28:29]
	v_pk_fma_f32 v[30:31], v[92:93], v[10:11], v[30:31]
	v_pk_fma_f32 v[32:33], v[86:87], v[12:13], v[32:33]
	v_pk_fma_f32 v[34:35], v[88:89], v[14:15], v[34:35]
	v_pk_fma_f32 v[36:37], v[82:83], v[16:17], v[36:37]
	v_pk_fma_f32 v[38:39], v[84:85], v[18:19], v[38:39]
	v_cvt_pk_bf16_f32 v24, v24, v25
	v_cvt_pk_bf16_f32 v25, v26, v27
	v_cvt_pk_bf16_f32 v26, v28, v29
	v_cvt_pk_bf16_f32 v27, v30, v31
	v_cvt_pk_bf16_f32 v28, v32, v33
	v_cvt_pk_bf16_f32 v29, v34, v35
	v_cvt_pk_bf16_f32 v30, v36, v37
	v_cvt_pk_bf16_f32 v31, v38, v39
	s_nop 0
	global_store_dwordx4 v63, v[24:27], s[72:73]
	global_store_dwordx4 v63, v[28:31], s[72:73] offset:16
	v_add_u32_e32 v63, 0x10000, v63
	s_waitcnt vmcnt(2)
	v_pk_fma_f32 v[40:41], v[78:79], v[4:5], v[40:41]
	v_pk_fma_f32 v[42:43], v[80:81], v[6:7], v[42:43]
	v_pk_fma_f32 v[44:45], v[74:75], v[8:9], v[44:45]
	v_pk_fma_f32 v[46:47], v[76:77], v[10:11], v[46:47]
	v_pk_fma_f32 v[48:49], v[70:71], v[12:13], v[48:49]
	v_pk_fma_f32 v[50:51], v[72:73], v[14:15], v[50:51]
	v_pk_fma_f32 v[52:53], v[66:67], v[16:17], v[52:53]
	v_pk_fma_f32 v[54:55], v[68:69], v[18:19], v[54:55]
	v_cvt_pk_bf16_f32 v40, v40, v41
	v_cvt_pk_bf16_f32 v41, v42, v43
	v_cvt_pk_bf16_f32 v42, v44, v45
	v_cvt_pk_bf16_f32 v43, v46, v47
	v_cvt_pk_bf16_f32 v44, v48, v49
	v_cvt_pk_bf16_f32 v45, v50, v51
	v_cvt_pk_bf16_f32 v46, v52, v53
	v_cvt_pk_bf16_f32 v47, v54, v55
	s_nop 0
	global_store_dwordx4 v63, v[40:43], s[72:73]
	global_store_dwordx4 v63, v[44:47], s[72:73] offset:16
	s_cbranch_vccnz .LBB0_440
	s_andn2_b64 vcc, exec, s[12:13]
	s_cbranch_vccnz .LBB0_439
	s_barrier
	s_branch .LBB0_439

; __device__ __forceinline__ unsigned xb_ld(unsigned* p)              { return __hip_atomic_load(p, __ATOMIC_RELAXED, __HIP_MEMORY_SCOPE_AGENT); }
; __device__ __forceinline__ unsigned xb_add(unsigned* p, unsigned v) { return __hip_atomic_fetch_add(p, v, __ATOMIC_RELAXED, __HIP_MEMORY_SCOPE_AGENT); }
; #define XB_SPIN(cond, bar) do { unsigned _sp = 0; while (cond) { __builtin_amdgcn_s_sleep(1); \
;     if ((++_sp & 255u) == 0u) { if (xb_ld(&(bar)[XB_TMO])) break; if (_sp > XB_SPIN_CAP) { atomicAdd(&(bar)[XB_TMO], 1u); break; } } } } while (0)
; __device__ __forceinline__ void xcd_barrier(const XcdBarrier& b) {
;     ...
;         if (nloc == 0u) { xcd_barrier_complete(bar, b.x, nloc, nx); b.st[0] = nloc; b.st[1] = nx; }
;         const unsigned old = xb_add(&bar[XB_XSUB(b.x)], 1u);
;         const unsigned gen = old / nloc;
;         if (old + 1u == (gen + 1u) * nloc) {
;             __builtin_amdgcn_fence(__ATOMIC_RELEASE, "agent");
;             asm volatile("s_waitcnt vmcnt(0)" ::: "memory");
;             const unsigned og = xb_add(&bar[XB_TOP], 1u);
;             const unsigned tg = og / nx;
;             if (og + 1u == (tg + 1u) * nx) xb_add(&bar[XB_TOPGEN], 1u);
;             else XB_SPIN(xb_ld(&bar[XB_TOPGEN]) == tg, bar);
;             __builtin_amdgcn_fence(__ATOMIC_ACQUIRE, "agent");
;             xb_add(&bar[XB_XGEN(b.x)], 1u);
;             asm volatile("s_waitcnt vmcnt(0)" ::: "memory");
;         } else {
;             XB_SPIN(xb_ld(&bar[XB_XGEN(b.x)]) == gen, bar);
.LBB0_490:
	s_lshl_b32 s4, s92, 8
	v_readlane_b32 s6, v255, 8
	v_readlane_b32 s7, v255, 9
	s_add_u32 s4, s6, s4
	s_addc_u32 s5, s7, 0
	v_mov_b32_e32 v2, 0x1000
	v_mov_b32_e32 v4, 1
	global_atomic_add v4, v2, v4, s[4:5] offset:1024 sc0
	v_cvt_f32_u32_e32 v2, v3
	v_sub_u32_e32 v5, 0, v3
	v_rcp_iflag_f32_e32 v2, v2
	s_nop 0
	v_mul_f32_e32 v2, 0x4f7ffffe, v2
	v_cvt_u32_f32_e32 v2, v2
	v_mul_lo_u32 v5, v5, v2
	v_mul_hi_u32 v5, v2, v5
	v_add_u32_e32 v2, v2, v5
	s_waitcnt vmcnt(0)
	v_mul_hi_u32 v2, v4, v2
	v_mul_lo_u32 v5, v2, v3
	v_sub_u32_e32 v5, v4, v5
	v_add_u32_e32 v6, 1, v2
	v_cmp_ge_u32_e32 vcc, v5, v3
	v_add_u32_e32 v4, 1, v4
	s_nop 0
	v_cndmask_b32_e32 v2, v2, v6, vcc
	v_sub_u32_e32 v6, v5, v3
	v_cndmask_b32_e32 v5, v5, v6, vcc
	v_add_u32_e32 v6, 1, v2
	v_cmp_ge_u32_e32 vcc, v5, v3
	s_nop 1
	v_cndmask_b32_e32 v2, v2, v6, vcc
	v_mul_lo_u32 v5, v3, v2
	v_add_u32_e32 v3, v5, v3
	v_cmp_ne_u32_e32 vcc, v4, v3
	s_and_saveexec_b64 s[6:7], vcc
	s_xor_b64 s[6:7], exec, s[6:7]
	s_cbranch_execz .LBB0_504
	s_waitcnt lgkmcnt(0)
	v_readlane_b32 s10, v255, 8
	v_readlane_b32 s11, v255, 9
	v_mov_b32_e32 v1, 0
	s_nop 3
	s_add_u32 s10, s10, 0x3500
	s_addc_u32 s11, s11, 0
	global_load_dword v1, v1, s[10:11] sc1
	s_waitcnt vmcnt(0)
	v_cmp_eq_u32_e32 vcc, v1, v2
	s_and_saveexec_b64 s[8:9], vcc
	s_cbranch_execz .LBB0_503
	s_mov_b32 s22, 1
	s_mov_b64 s[12:13], 0
	v_mov_b32_e32 v1, 0
	s_branch .LBB0_494

; __device__ __forceinline__ unsigned xb_ld(unsigned* p)              { return __hip_atomic_load(p, __ATOMIC_RELAXED, __HIP_MEMORY_SCOPE_AGENT); }
; __device__ __forceinline__ unsigned xb_add(unsigned* p, unsigned v) { return __hip_atomic_fetch_add(p, v, __ATOMIC_RELAXED, __HIP_MEMORY_SCOPE_AGENT); }
; #define XB_SPIN(cond, bar) do { unsigned _sp = 0; while (cond) { __builtin_amdgcn_s_sleep(1); \
;     if ((++_sp & 255u) == 0u) { if (xb_ld(&(bar)[XB_TMO])) break; if (_sp > XB_SPIN_CAP) { atomicAdd(&(bar)[XB_TMO], 1u); break; } } } } while (0)
; __device__ __forceinline__ void xcd_barrier(const XcdBarrier& b) {
;     ...
;         if (nloc == 0u) { xcd_barrier_complete(bar, b.x, nloc, nx); b.st[0] = nloc; b.st[1] = nx; }
;         const unsigned old = xb_add(&bar[XB_XSUB(b.x)], 1u);
;         const unsigned gen = old / nloc;
;         if (old + 1u == (gen + 1u) * nloc) {
;             __builtin_amdgcn_fence(__ATOMIC_RELEASE, "agent");
;             asm volatile("s_waitcnt vmcnt(0)" ::: "memory");
;             const unsigned og = xb_add(&bar[XB_TOP], 1u);
;             const unsigned tg = og / nx;
;             if (og + 1u == (tg + 1u) * nx) xb_add(&bar[XB_TOPGEN], 1u);
;             else XB_SPIN(xb_ld(&bar[XB_TOPGEN]) == tg, bar);
;             __builtin_amdgcn_fence(__ATOMIC_ACQUIRE, "agent");
;             xb_add(&bar[XB_XGEN(b.x)], 1u);
;             asm volatile("s_waitcnt vmcnt(0)" ::: "memory");
;         } else {
;             XB_SPIN(xb_ld(&bar[XB_XGEN(b.x)]) == gen, bar);
.LBB0_804:
	s_lshl_b32 s2, s92, 8
	v_readlane_b32 s4, v255, 8
	v_readlane_b32 s5, v255, 9
	s_add_u32 s2, s4, s2
	s_addc_u32 s3, s5, 0
	v_mov_b32_e32 v2, 0x1000
	v_mov_b32_e32 v4, 1
	global_atomic_add v4, v2, v4, s[2:3] offset:1024 sc0
	v_cvt_f32_u32_e32 v2, v3
	v_sub_u32_e32 v5, 0, v3
	v_rcp_iflag_f32_e32 v2, v2
	s_nop 0
	v_mul_f32_e32 v2, 0x4f7ffffe, v2
	v_cvt_u32_f32_e32 v2, v2
	v_mul_lo_u32 v5, v5, v2
	v_mul_hi_u32 v5, v2, v5
	v_add_u32_e32 v2, v2, v5
	s_waitcnt vmcnt(0)
	v_mul_hi_u32 v2, v4, v2
	v_mul_lo_u32 v5, v2, v3
	v_sub_u32_e32 v5, v4, v5
	v_add_u32_e32 v6, 1, v2
	v_cmp_ge_u32_e32 vcc, v5, v3
	v_add_u32_e32 v4, 1, v4
	s_nop 0
	v_cndmask_b32_e32 v2, v2, v6, vcc
	v_sub_u32_e32 v6, v5, v3
	v_cndmask_b32_e32 v5, v5, v6, vcc
	v_add_u32_e32 v6, 1, v2
	v_cmp_ge_u32_e32 vcc, v5, v3
	s_nop 1
	v_cndmask_b32_e32 v2, v2, v6, vcc
	v_mul_lo_u32 v5, v3, v2
	v_add_u32_e32 v3, v5, v3
	v_cmp_ne_u32_e32 vcc, v4, v3
	s_and_saveexec_b64 s[4:5], vcc
	s_xor_b64 s[4:5], exec, s[4:5]
	s_cbranch_execz .LBB0_818
	s_waitcnt lgkmcnt(0)
	v_readlane_b32 s8, v255, 8
	v_readlane_b32 s9, v255, 9
	v_mov_b32_e32 v1, 0
	s_nop 3
	s_add_u32 s8, s8, 0x3500
	s_addc_u32 s9, s9, 0
	global_load_dword v1, v1, s[8:9] sc1
	s_waitcnt vmcnt(0)
	v_cmp_eq_u32_e32 vcc, v1, v2
	s_and_saveexec_b64 s[6:7], vcc
	s_cbranch_execz .LBB0_817
	s_mov_b32 s20, 1
	s_mov_b64 s[10:11], 0
	v_mov_b32_e32 v1, 0
	s_branch .LBB0_808

; __device__ __forceinline__ unsigned xb_ld(unsigned* p)              { return __hip_atomic_load(p, __ATOMIC_RELAXED, __HIP_MEMORY_SCOPE_AGENT); }
; __device__ __forceinline__ unsigned xb_add(unsigned* p, unsigned v) { return __hip_atomic_fetch_add(p, v, __ATOMIC_RELAXED, __HIP_MEMORY_SCOPE_AGENT); }
; #define XB_SPIN(cond, bar) do { unsigned _sp = 0; while (cond) { __builtin_amdgcn_s_sleep(1); \
;     if ((++_sp & 255u) == 0u) { if (xb_ld(&(bar)[XB_TMO])) break; if (_sp > XB_SPIN_CAP) { atomicAdd(&(bar)[XB_TMO], 1u); break; } } } } while (0)
; __device__ __forceinline__ void xcd_barrier(const XcdBarrier& b) {
;     ...
;             const unsigned og = xb_add(&bar[XB_TOP], 1u);
;             const unsigned tg = og / nx;
;             if (og + 1u == (tg + 1u) * nx) xb_add(&bar[XB_TOPGEN], 1u);
;             else XB_SPIN(xb_ld(&bar[XB_TOPGEN]) == tg, bar);
;             __builtin_amdgcn_fence(__ATOMIC_ACQUIRE, "agent");
;             xb_add(&bar[XB_XGEN(b.x)], 1u);
;             asm volatile("s_waitcnt vmcnt(0)" ::: "memory");
.LBB0_835:
	s_or_b64 exec, exec, s[4:5]
	v_mov_b32_e32 v1, 0x2000
	v_mov_b32_e32 v2, 1
	s_waitcnt vmcnt(0)
	buffer_inv sc1
	s_waitcnt vmcnt(0)

; __device__ __forceinline__ unsigned cvt_pk_bf16(float lo, float hi) { unsigned r; asm volatile("v_cvt_pk_bf16_f32 %0, %1, %2" : "=v"(r) : "v"(lo), "v"(hi)); return r; }
; __device__ __forceinline__ float bf_lo(unsigned w) { return __uint_as_float(w << 16); }
; __device__ __forceinline__ float bf_hi(unsigned w) { return __uint_as_float(w & 0xffff0000u); }
;     __device__ __forceinline__ void operator()(const f32x4 (&acc)[2][2][4][2], const Unit& u, int wr, int wc, int fr, int fq) const {
;         const int row0 = u.pm * BM + wr * 64 + fr, col0 = u.pn * BM + wc * 64 + 16 * fq;
;         const float* gp = gate + (size_t)((u.pm * BM) / S) * MODW + col0;
;         f32x4 gv[4];
; #pragma unroll
;         for (int q = 0; q < 4; ++q) gv[q] = *(const f32x4*)(gp + 4 * q) * sc;
; #pragma unroll
;         for (int ai = 0; ai < 2; ++ai)
; #pragma unroll
;             for (int m = 0; m < 4; ++m) { const size_t off = (size_t)(row0 + ai * HALF + m * 16) * D + col0; f32x4 r[4];
;                 if (RBF) { const u32x4 w0 = *(const u32x4*)((const bf16_t*)R + off), w1 = *(const u32x4*)((const bf16_t*)R + off + 8);
;                     r[0] = (f32x4){bf_lo(w0.x), bf_hi(w0.x), bf_lo(w0.y), bf_hi(w0.y)}; r[1] = (f32x4){bf_lo(w0.z), bf_hi(w0.z), bf_lo(w0.w), bf_hi(w0.w)};
;                     r[2] = (f32x4){bf_lo(w1.x), bf_hi(w1.x), bf_lo(w1.y), bf_hi(w1.y)}; r[3] = (f32x4){bf_lo(w1.z), bf_hi(w1.z), bf_lo(w1.w), bf_hi(w1.w)}; }
;                 else {
; #pragma unroll
;                     for (int q = 0; q < 4; ++q) r[q] = *(const f32x4*)((const float*)R + off + 4 * q); }
; #pragma unroll
;                 for (int q = 0; q < 4; ++q) r[q] = r[q] + gv[q] * acc[ai][q >> 1][m][q & 1];
;                 u32x4 o0, o1; o0.x = cvt_pk_bf16(r[0][0], r[0][1]); o0.y = cvt_pk_bf16(r[0][2], r[0][3]); o0.z = cvt_pk_bf16(r[1][0], r[1][1]); o0.w = cvt_pk_bf16(r[1][2], r[1][3]);
;                 o1.x = cvt_pk_bf16(r[2][0], r[2][1]); o1.y = cvt_pk_bf16(r[2][2], r[2][3]); o1.z = cvt_pk_bf16(r[3][0], r[3][1]); o1.w = cvt_pk_bf16(r[3][2], r[3][3]);
;                 *(u32x4*)(out + off) = o0; *(u32x4*)(out + off + 8) = o1; }
.LBB0_1236:
	v_lshl_add_u32 v22, s62, 8, v1
	s_ashr_i32 s24, s62, 31
	v_lshl_or_b32 v20, s63, 8, v244
	v_ashrrev_i32_e32 v23, 31, v22
	s_lshr_b32 s24, s24, 28
	v_ashrrev_i32_e32 v21, 31, v20
	v_lshlrev_b64 v[2:3], 11, v[22:23]
	s_add_i32 s24, s62, s24
	v_lshl_add_u64 v[2:3], v[2:3], 0, v[20:21]
	s_ashr_i32 s24, s24, 4
	v_lshlrev_b64 v[18:19], 1, v[2:3]
	s_mul_hi_i32 s25, s24, 0xc000
	s_mul_i32 s24, s24, 0xc000
	s_nop 15
	s_nop 7
	s_add_u32 s24, s47, s24
	s_addc_u32 s25, s48, s25
	v_lshlrev_b32_e32 v2, 2, v20
	v_lshlrev_b32_e32 v3, 11, v22
	global_load_dwordx4 v[4:7], v2, s[24:25]
	global_load_dwordx4 v[8:11], v2, s[24:25] offset:16
	global_load_dwordx4 v[12:15], v2, s[24:25] offset:32
	global_load_dwordx4 v[16:19], v2, s[24:25] offset:48
	v_add_u32_e32 v3, v3, v20
	v_lshlrev_b32_e32 v3, 1, v3
	v_mov_b32_e32 v22, v3
	global_load_dwordx4 v[24:27], v3, s[12:13]
	global_load_dwordx4 v[28:31], v3, s[12:13] offset:16
	v_add_u32_e32 v3, 0x10000, v3
	global_load_dwordx4 v[32:35], v3, s[12:13]
	global_load_dwordx4 v[36:39], v3, s[12:13] offset:16
	v_add_u32_e32 v3, 0x10000, v3
	global_load_dwordx4 v[40:43], v3, s[12:13]
	global_load_dwordx4 v[44:47], v3, s[12:13] offset:16
	s_and_b64 vcc, exec, s[0:1]
	s_mov_b64 s[0:1], -1
	s_waitcnt vmcnt(6)
	v_pk_mul_f32 v[4:5], v[4:5], s[18:19] op_sel_hi:[1,0]
	v_pk_mul_f32 v[6:7], v[6:7], s[18:19] op_sel_hi:[1,0]
	v_pk_mul_f32 v[8:9], v[8:9], s[18:19] op_sel_hi:[1,0]
	v_pk_mul_f32 v[10:11], v[10:11], s[18:19] op_sel_hi:[1,0]
	v_pk_mul_f32 v[12:13], v[12:13], s[18:19] op_sel_hi:[1,0]
	v_pk_mul_f32 v[14:15], v[14:15], s[18:19] op_sel_hi:[1,0]
	v_pk_mul_f32 v[16:17], v[16:17], s[18:19] op_sel_hi:[1,0]
	v_pk_mul_f32 v[18:19], v[18:19], s[18:19] op_sel_hi:[1,0]
	s_waitcnt vmcnt(4)
	v_lshlrev_b32_e32 v48, 16, v24
	v_and_b32_e32 v49, 0xffff0000, v24
	v_lshlrev_b32_e32 v50, 16, v25
	v_and_b32_e32 v51, 0xffff0000, v25
	v_lshlrev_b32_e32 v52, 16, v26
	v_and_b32_e32 v53, 0xffff0000, v26
	v_lshlrev_b32_e32 v54, 16, v27
	v_and_b32_e32 v55, 0xffff0000, v27
	v_lshlrev_b32_e32 v56, 16, v28
	v_and_b32_e32 v57, 0xffff0000, v28
	v_lshlrev_b32_e32 v58, 16, v29
	v_and_b32_e32 v59, 0xffff0000, v29
	v_lshlrev_b32_e32 v60, 16, v30
	v_and_b32_e32 v61, 0xffff0000, v30
	v_lshlrev_b32_e32 v62, 16, v31
	v_and_b32_e32 v63, 0xffff0000, v31
	v_pk_fma_f32 v[48:49], v[190:191], v[4:5], v[48:49]
	v_pk_fma_f32 v[50:51], v[192:193], v[6:7], v[50:51]
	v_pk_fma_f32 v[52:53], v[186:187], v[8:9], v[52:53]
	v_pk_fma_f32 v[54:55], v[188:189], v[10:11], v[54:55]
	v_pk_fma_f32 v[56:57], v[182:183], v[12:13], v[56:57]
	v_pk_fma_f32 v[58:59], v[184:185], v[14:15], v[58:59]
	v_pk_fma_f32 v[60:61], v[178:179], v[16:17], v[60:61]
	v_pk_fma_f32 v[62:63], v[180:181], v[18:19], v[62:63]
	v_cvt_pk_bf16_f32 v48, v48, v49
	v_cvt_pk_bf16_f32 v49, v50, v51
	v_cvt_pk_bf16_f32 v50, v52, v53
	v_cvt_pk_bf16_f32 v51, v54, v55
	v_cvt_pk_bf16_f32 v52, v56, v57
	v_cvt_pk_bf16_f32 v53, v58, v59
	v_cvt_pk_bf16_f32 v54, v60, v61
	v_cvt_pk_bf16_f32 v55, v62, v63
	s_nop 0
	global_store_dwordx4 v22, v[48:51], s[72:73]
	global_store_dwordx4 v22, v[52:55], s[72:73] offset:16
	v_add_u32_e32 v22, 0x10000, v22
	v_add_u32_e32 v3, 0x10000, v3
	global_load_dwordx4 v[24:27], v3, s[12:13]
	global_load_dwordx4 v[28:31], v3, s[12:13] offset:16
	s_waitcnt vmcnt(6)
	v_lshlrev_b32_e32 v48, 16, v32
	v_and_b32_e32 v49, 0xffff0000, v32
	v_lshlrev_b32_e32 v50, 16, v33
	v_and_b32_e32 v51, 0xffff0000, v33
	v_lshlrev_b32_e32 v52, 16, v34
	v_and_b32_e32 v53, 0xffff0000, v34
	v_lshlrev_b32_e32 v54, 16, v35
	v_and_b32_e32 v55, 0xffff0000, v35
	v_lshlrev_b32_e32 v56, 16, v36
	v_and_b32_e32 v57, 0xffff0000, v36
	v_lshlrev_b32_e32 v58, 16, v37
	v_and_b32_e32 v59, 0xffff0000, v37
	v_lshlrev_b32_e32 v60, 16, v38
	v_and_b32_e32 v61, 0xffff0000, v38
	v_lshlrev_b32_e32 v62, 16, v39
	v_and_b32_e32 v63, 0xffff0000, v39
	v_pk_fma_f32 v[48:49], v[174:175], v[4:5], v[48:49]
	v_pk_fma_f32 v[50:51], v[176:177], v[6:7], v[50:51]
	v_pk_fma_f32 v[52:53], v[170:171], v[8:9], v[52:53]
	v_pk_fma_f32 v[54:55], v[172:173], v[10:11], v[54:55]
	v_pk_fma_f32 v[56:57], v[166:167], v[12:13], v[56:57]
	v_pk_fma_f32 v[58:59], v[168:169], v[14:15], v[58:59]
	v_pk_fma_f32 v[60:61], v[162:163], v[16:17], v[60:61]
	v_pk_fma_f32 v[62:63], v[164:165], v[18:19], v[62:63]
	v_cvt_pk_bf16_f32 v48, v48, v49
	v_cvt_pk_bf16_f32 v49, v50, v51
	v_cvt_pk_bf16_f32 v50, v52, v53
	v_cvt_pk_bf16_f32 v51, v54, v55
	v_cvt_pk_bf16_f32 v52, v56, v57
	v_cvt_pk_bf16_f32 v53, v58, v59
	v_cvt_pk_bf16_f32 v54, v60, v61
	v_cvt_pk_bf16_f32 v55, v62, v63
	s_nop 0
	global_store_dwordx4 v22, v[48:51], s[72:73]
	global_store_dwordx4 v22, v[52:55], s[72:73] offset:16
	v_add_u32_e32 v22, 0x10000, v22
	v_add_u32_e32 v3, 0x50000, v3
	global_load_dwordx4 v[32:35], v3, s[12:13]
	global_load_dwordx4 v[36:39], v3, s[12:13] offset:16
	s_waitcnt vmcnt(8)
	v_lshlrev_b32_e32 v48, 16, v40
	v_and_b32_e32 v49, 0xffff0000, v40
	v_lshlrev_b32_e32 v50, 16, v41
	v_and_b32_e32 v51, 0xffff0000, v41
	v_lshlrev_b32_e32 v52, 16, v42
	v_and_b32_e32 v53, 0xffff0000, v42
	v_lshlrev_b32_e32 v54, 16, v43
	v_and_b32_e32 v55, 0xffff0000, v43
	v_lshlrev_b32_e32 v56, 16, v44
	v_and_b32_e32 v57, 0xffff0000, v44
	v_lshlrev_b32_e32 v58, 16, v45
	v_and_b32_e32 v59, 0xffff0000, v45
	v_lshlrev_b32_e32 v60, 16, v46
	v_and_b32_e32 v61, 0xffff0000, v46
	v_lshlrev_b32_e32 v62, 16, v47
	v_and_b32_e32 v63, 0xffff0000, v47
	v_pk_fma_f32 v[48:49], v[158:159], v[4:5], v[48:49]
	v_pk_fma_f32 v[50:51], v[160:161], v[6:7], v[50:51]
	v_pk_fma_f32 v[52:53], v[154:155], v[8:9], v[52:53]
	v_pk_fma_f32 v[54:55], v[156:157], v[10:11], v[54:55]
	v_pk_fma_f32 v[56:57], v[150:151], v[12:13], v[56:57]
	v_pk_fma_f32 v[58:59], v[152:153], v[14:15], v[58:59]
	v_pk_fma_f32 v[60:61], v[146:147], v[16:17], v[60:61]
	v_pk_fma_f32 v[62:63], v[148:149], v[18:19], v[62:63]
	v_cvt_pk_bf16_f32 v48, v48, v49
	v_cvt_pk_bf16_f32 v49, v50, v51
	v_cvt_pk_bf16_f32 v50, v52, v53
	v_cvt_pk_bf16_f32 v51, v54, v55
	v_cvt_pk_bf16_f32 v52, v56, v57
	v_cvt_pk_bf16_f32 v53, v58, v59
	v_cvt_pk_bf16_f32 v54, v60, v61
	v_cvt_pk_bf16_f32 v55, v62, v63
	s_nop 0
	global_store_dwordx4 v22, v[48:51], s[72:73]
	global_store_dwordx4 v22, v[52:55], s[72:73] offset:16
	v_add_u32_e32 v22, 0x10000, v22
	v_add_u32_e32 v3, 0x10000, v3
	global_load_dwordx4 v[40:43], v3, s[12:13]
	global_load_dwordx4 v[44:47], v3, s[12:13] offset:16
	s_waitcnt vmcnt(8)
; __device__ __forceinline__ unsigned cvt_pk_bf16(float lo, float hi) { unsigned r; asm volatile("v_cvt_pk_bf16_f32 %0, %1, %2" : "=v"(r) : "v"(lo), "v"(hi)); return r; }
; __device__ __forceinline__ float bf_lo(unsigned w) { return __uint_as_float(w << 16); }
; __device__ __forceinline__ float bf_hi(unsigned w) { return __uint_as_float(w & 0xffff0000u); }
;     __device__ __forceinline__ void operator()(const f32x4 (&acc)[2][2][4][2], const Unit& u, int wr, int wc, int fr, int fq) const {
;     ...
;         for (int ai = 0; ai < 2; ++ai)
; #pragma unroll
;             for (int m = 0; m < 4; ++m) { const size_t off = (size_t)(row0 + ai * HALF + m * 16) * D + col0; f32x4 r[4];
;                 if (RBF) { const u32x4 w0 = *(const u32x4*)((const bf16_t*)R + off), w1 = *(const u32x4*)((const bf16_t*)R + off + 8);
;                     r[0] = (f32x4){bf_lo(w0.x), bf_hi(w0.x), bf_lo(w0.y), bf_hi(w0.y)}; r[1] = (f32x4){bf_lo(w0.z), bf_hi(w0.z), bf_lo(w0.w), bf_hi(w0.w)};
;                     r[2] = (f32x4){bf_lo(w1.x), bf_hi(w1.x), bf_lo(w1.y), bf_hi(w1.y)}; r[3] = (f32x4){bf_lo(w1.z), bf_hi(w1.z), bf_lo(w1.w), bf_hi(w1.w)}; }
;                 else {
; #pragma unroll
;                     for (int q = 0; q < 4; ++q) r[q] = *(const f32x4*)((const float*)R + off + 4 * q); }
; #pragma unroll
;                 for (int q = 0; q < 4; ++q) r[q] = r[q] + gv[q] * acc[ai][q >> 1][m][q & 1];
;                 u32x4 o0, o1; o0.x = cvt_pk_bf16(r[0][0], r[0][1]); o0.y = cvt_pk_bf16(r[0][2], r[0][3]); o0.z = cvt_pk_bf16(r[1][0], r[1][1]); o0.w = cvt_pk_bf16(r[1][2], r[1][3]);
;                 o1.x = cvt_pk_bf16(r[2][0], r[2][1]); o1.y = cvt_pk_bf16(r[2][2], r[2][3]); o1.z = cvt_pk_bf16(r[3][0], r[3][1]); o1.w = cvt_pk_bf16(r[3][2], r[3][3]);
;                 *(u32x4*)(out + off) = o0; *(u32x4*)(out + off + 8) = o1; }
	v_lshlrev_b32_e32 v48, 16, v24
	v_and_b32_e32 v49, 0xffff0000, v24
	v_lshlrev_b32_e32 v50, 16, v25
	v_and_b32_e32 v51, 0xffff0000, v25
	v_lshlrev_b32_e32 v52, 16, v26
	v_and_b32_e32 v53, 0xffff0000, v26
	v_lshlrev_b32_e32 v54, 16, v27
	v_and_b32_e32 v55, 0xffff0000, v27
	v_lshlrev_b32_e32 v56, 16, v28
	v_and_b32_e32 v57, 0xffff0000, v28
	v_lshlrev_b32_e32 v58, 16, v29
	v_and_b32_e32 v59, 0xffff0000, v29
	v_lshlrev_b32_e32 v60, 16, v30
	v_and_b32_e32 v61, 0xffff0000, v30
	v_lshlrev_b32_e32 v62, 16, v31
	v_and_b32_e32 v63, 0xffff0000, v31
	v_pk_fma_f32 v[48:49], v[142:143], v[4:5], v[48:49]
	v_pk_fma_f32 v[50:51], v[144:145], v[6:7], v[50:51]
	v_pk_fma_f32 v[52:53], v[138:139], v[8:9], v[52:53]
	v_pk_fma_f32 v[54:55], v[140:141], v[10:11], v[54:55]
	v_pk_fma_f32 v[56:57], v[134:135], v[12:13], v[56:57]
	v_pk_fma_f32 v[58:59], v[136:137], v[14:15], v[58:59]
	v_pk_fma_f32 v[60:61], v[130:131], v[16:17], v[60:61]
	v_pk_fma_f32 v[62:63], v[132:133], v[18:19], v[62:63]
	v_cvt_pk_bf16_f32 v48, v48, v49
	v_cvt_pk_bf16_f32 v49, v50, v51
	v_cvt_pk_bf16_f32 v50, v52, v53
	v_cvt_pk_bf16_f32 v51, v54, v55
	v_cvt_pk_bf16_f32 v52, v56, v57
	v_cvt_pk_bf16_f32 v53, v58, v59
	v_cvt_pk_bf16_f32 v54, v60, v61
	v_cvt_pk_bf16_f32 v55, v62, v63
	s_nop 0
	global_store_dwordx4 v22, v[48:51], s[72:73]
	global_store_dwordx4 v22, v[52:55], s[72:73] offset:16
	v_add_u32_e32 v22, 0x50000, v22
	v_add_u32_e32 v3, 0x10000, v3
	global_load_dwordx4 v[24:27], v3, s[12:13]
	global_load_dwordx4 v[28:31], v3, s[12:13] offset:16
	s_waitcnt vmcnt(8)
	v_lshlrev_b32_e32 v48, 16, v32
	v_and_b32_e32 v49, 0xffff0000, v32
	v_lshlrev_b32_e32 v50, 16, v33
	v_and_b32_e32 v51, 0xffff0000, v33
	v_lshlrev_b32_e32 v52, 16, v34
	v_and_b32_e32 v53, 0xffff0000, v34
	v_lshlrev_b32_e32 v54, 16, v35
	v_and_b32_e32 v55, 0xffff0000, v35
	v_lshlrev_b32_e32 v56, 16, v36
	v_and_b32_e32 v57, 0xffff0000, v36
	v_lshlrev_b32_e32 v58, 16, v37
	v_and_b32_e32 v59, 0xffff0000, v37
	v_lshlrev_b32_e32 v60, 16, v38
	v_and_b32_e32 v61, 0xffff0000, v38
	v_lshlrev_b32_e32 v62, 16, v39
	v_and_b32_e32 v63, 0xffff0000, v39
	v_pk_fma_f32 v[48:49], v[126:127], v[4:5], v[48:49]
	v_pk_fma_f32 v[50:51], v[128:129], v[6:7], v[50:51]
	v_pk_fma_f32 v[52:53], v[122:123], v[8:9], v[52:53]
	v_pk_fma_f32 v[54:55], v[124:125], v[10:11], v[54:55]
	v_pk_fma_f32 v[56:57], v[118:119], v[12:13], v[56:57]
	v_pk_fma_f32 v[58:59], v[120:121], v[14:15], v[58:59]
	v_pk_fma_f32 v[60:61], v[114:115], v[16:17], v[60:61]
	v_pk_fma_f32 v[62:63], v[116:117], v[18:19], v[62:63]
	v_cvt_pk_bf16_f32 v48, v48, v49
	v_cvt_pk_bf16_f32 v49, v50, v51
	v_cvt_pk_bf16_f32 v50, v52, v53
	v_cvt_pk_bf16_f32 v51, v54, v55
	v_cvt_pk_bf16_f32 v52, v56, v57
	v_cvt_pk_bf16_f32 v53, v58, v59
	v_cvt_pk_bf16_f32 v54, v60, v61
	v_cvt_pk_bf16_f32 v55, v62, v63
	s_nop 0
	global_store_dwordx4 v22, v[48:51], s[72:73]
	global_store_dwordx4 v22, v[52:55], s[72:73] offset:16
	v_add_u32_e32 v22, 0x10000, v22
	v_add_u32_e32 v3, 0x10000, v3
	global_load_dwordx4 v[32:35], v3, s[12:13]
	global_load_dwordx4 v[36:39], v3, s[12:13] offset:16
	s_waitcnt vmcnt(8)
; __device__ __forceinline__ unsigned cvt_pk_bf16(float lo, float hi) { unsigned r; asm volatile("v_cvt_pk_bf16_f32 %0, %1, %2" : "=v"(r) : "v"(lo), "v"(hi)); return r; }
; __device__ __forceinline__ float bf_lo(unsigned w) { return __uint_as_float(w << 16); }
; __device__ __forceinline__ float bf_hi(unsigned w) { return __uint_as_float(w & 0xffff0000u); }
;     __device__ __forceinline__ void operator()(const f32x4 (&acc)[2][2][4][2], const Unit& u, int wr, int wc, int fr, int fq) const {
;     ...
;         for (int ai = 0; ai < 2; ++ai)
; #pragma unroll
;             for (int m = 0; m < 4; ++m) { const size_t off = (size_t)(row0 + ai * HALF + m * 16) * D + col0; f32x4 r[4];
;                 if (RBF) { const u32x4 w0 = *(const u32x4*)((const bf16_t*)R + off), w1 = *(const u32x4*)((const bf16_t*)R + off + 8);
;                     r[0] = (f32x4){bf_lo(w0.x), bf_hi(w0.x), bf_lo(w0.y), bf_hi(w0.y)}; r[1] = (f32x4){bf_lo(w0.z), bf_hi(w0.z), bf_lo(w0.w), bf_hi(w0.w)};
;                     r[2] = (f32x4){bf_lo(w1.x), bf_hi(w1.x), bf_lo(w1.y), bf_hi(w1.y)}; r[3] = (f32x4){bf_lo(w1.z), bf_hi(w1.z), bf_lo(w1.w), bf_hi(w1.w)}; }
;                 else {
; #pragma unroll
;                     for (int q = 0; q < 4; ++q) r[q] = *(const f32x4*)((const float*)R + off + 4 * q); }
; #pragma unroll
;                 for (int q = 0; q < 4; ++q) r[q] = r[q] + gv[q] * acc[ai][q >> 1][m][q & 1];
;                 u32x4 o0, o1; o0.x = cvt_pk_bf16(r[0][0], r[0][1]); o0.y = cvt_pk_bf16(r[0][2], r[0][3]); o0.z = cvt_pk_bf16(r[1][0], r[1][1]); o0.w = cvt_pk_bf16(r[1][2], r[1][3]);
;                 o1.x = cvt_pk_bf16(r[2][0], r[2][1]); o1.y = cvt_pk_bf16(r[2][2], r[2][3]); o1.z = cvt_pk_bf16(r[3][0], r[3][1]); o1.w = cvt_pk_bf16(r[3][2], r[3][3]);
;                 *(u32x4*)(out + off) = o0; *(u32x4*)(out + off + 8) = o1; }
	v_lshlrev_b32_e32 v48, 16, v40
	v_and_b32_e32 v49, 0xffff0000, v40
	v_lshlrev_b32_e32 v50, 16, v41
	v_and_b32_e32 v51, 0xffff0000, v41
	v_lshlrev_b32_e32 v52, 16, v42
	v_and_b32_e32 v53, 0xffff0000, v42
	v_lshlrev_b32_e32 v54, 16, v43
	v_and_b32_e32 v55, 0xffff0000, v43
	v_lshlrev_b32_e32 v56, 16, v44
	v_and_b32_e32 v57, 0xffff0000, v44
	v_lshlrev_b32_e32 v58, 16, v45
	v_and_b32_e32 v59, 0xffff0000, v45
	v_lshlrev_b32_e32 v60, 16, v46
	v_and_b32_e32 v61, 0xffff0000, v46
	v_lshlrev_b32_e32 v62, 16, v47
	v_and_b32_e32 v63, 0xffff0000, v47
	v_pk_fma_f32 v[48:49], v[110:111], v[4:5], v[48:49]
	v_pk_fma_f32 v[50:51], v[112:113], v[6:7], v[50:51]
	v_pk_fma_f32 v[52:53], v[106:107], v[8:9], v[52:53]
	v_pk_fma_f32 v[54:55], v[108:109], v[10:11], v[54:55]
	v_pk_fma_f32 v[56:57], v[102:103], v[12:13], v[56:57]
	v_pk_fma_f32 v[58:59], v[104:105], v[14:15], v[58:59]
	v_pk_fma_f32 v[60:61], v[98:99], v[16:17], v[60:61]
	v_pk_fma_f32 v[62:63], v[100:101], v[18:19], v[62:63]
	v_cvt_pk_bf16_f32 v48, v48, v49
	v_cvt_pk_bf16_f32 v49, v50, v51
	v_cvt_pk_bf16_f32 v50, v52, v53
	v_cvt_pk_bf16_f32 v51, v54, v55
	v_cvt_pk_bf16_f32 v52, v56, v57
	v_cvt_pk_bf16_f32 v53, v58, v59
	v_cvt_pk_bf16_f32 v54, v60, v61
	v_cvt_pk_bf16_f32 v55, v62, v63
	s_nop 0
	global_store_dwordx4 v22, v[48:51], s[72:73]
	global_store_dwordx4 v22, v[52:55], s[72:73] offset:16
	v_add_u32_e32 v22, 0x10000, v22
	s_waitcnt vmcnt(6)
	v_lshlrev_b32_e32 v48, 16, v24
	v_and_b32_e32 v49, 0xffff0000, v24
	v_lshlrev_b32_e32 v50, 16, v25
	v_and_b32_e32 v51, 0xffff0000, v25
	v_lshlrev_b32_e32 v52, 16, v26
	v_and_b32_e32 v53, 0xffff0000, v26
	v_lshlrev_b32_e32 v54, 16, v27
	v_and_b32_e32 v55, 0xffff0000, v27
	v_lshlrev_b32_e32 v56, 16, v28
	v_and_b32_e32 v57, 0xffff0000, v28
	v_lshlrev_b32_e32 v58, 16, v29
	v_and_b32_e32 v59, 0xffff0000, v29
	v_lshlrev_b32_e32 v60, 16, v30
	v_and_b32_e32 v61, 0xffff0000, v30
	v_lshlrev_b32_e32 v62, 16, v31
	v_and_b32_e32 v63, 0xffff0000, v31
	v_pk_fma_f32 v[48:49], v[94:95], v[4:5], v[48:49]
	v_pk_fma_f32 v[50:51], v[96:97], v[6:7], v[50:51]
	v_pk_fma_f32 v[52:53], v[90:91], v[8:9], v[52:53]
	v_pk_fma_f32 v[54:55], v[92:93], v[10:11], v[54:55]
	v_pk_fma_f32 v[56:57], v[86:87], v[12:13], v[56:57]
	v_pk_fma_f32 v[58:59], v[88:89], v[14:15], v[58:59]
	v_pk_fma_f32 v[60:61], v[82:83], v[16:17], v[60:61]
	v_pk_fma_f32 v[62:63], v[84:85], v[18:19], v[62:63]
	v_cvt_pk_bf16_f32 v48, v48, v49
	v_cvt_pk_bf16_f32 v49, v50, v51
	v_cvt_pk_bf16_f32 v50, v52, v53
	v_cvt_pk_bf16_f32 v51, v54, v55
	v_cvt_pk_bf16_f32 v52, v56, v57
	v_cvt_pk_bf16_f32 v53, v58, v59
	v_cvt_pk_bf16_f32 v54, v60, v61
	v_cvt_pk_bf16_f32 v55, v62, v63
	s_nop 0
	global_store_dwordx4 v22, v[48:51], s[72:73]
	global_store_dwordx4 v22, v[52:55], s[72:73] offset:16
	v_add_u32_e32 v22, 0x10000, v22
	s_waitcnt vmcnt(4)
	v_lshlrev_b32_e32 v48, 16, v32
	v_and_b32_e32 v49, 0xffff0000, v32
	v_lshlrev_b32_e32 v50, 16, v33
	v_and_b32_e32 v51, 0xffff0000, v33
	v_lshlrev_b32_e32 v52, 16, v34
	v_and_b32_e32 v53, 0xffff0000, v34
	v_lshlrev_b32_e32 v54, 16, v35
	v_and_b32_e32 v55, 0xffff0000, v35
	v_lshlrev_b32_e32 v56, 16, v36
	v_and_b32_e32 v57, 0xffff0000, v36
	v_lshlrev_b32_e32 v58, 16, v37
	v_and_b32_e32 v59, 0xffff0000, v37
	v_lshlrev_b32_e32 v60, 16, v38
	v_and_b32_e32 v61, 0xffff0000, v38
	v_lshlrev_b32_e32 v62, 16, v39
	v_and_b32_e32 v63, 0xffff0000, v39
	v_pk_fma_f32 v[48:49], v[78:79], v[4:5], v[48:49]
	v_pk_fma_f32 v[50:51], v[80:81], v[6:7], v[50:51]
	v_pk_fma_f32 v[52:53], v[74:75], v[8:9], v[52:53]
	v_pk_fma_f32 v[54:55], v[76:77], v[10:11], v[54:55]
	v_pk_fma_f32 v[56:57], v[70:71], v[12:13], v[56:57]
	v_pk_fma_f32 v[58:59], v[72:73], v[14:15], v[58:59]
	v_pk_fma_f32 v[60:61], v[66:67], v[16:17], v[60:61]
	v_pk_fma_f32 v[62:63], v[68:69], v[18:19], v[62:63]
	v_cvt_pk_bf16_f32 v48, v48, v49
	v_cvt_pk_bf16_f32 v49, v50, v51
	v_cvt_pk_bf16_f32 v50, v52, v53
	v_cvt_pk_bf16_f32 v51, v54, v55
	v_cvt_pk_bf16_f32 v52, v56, v57
	v_cvt_pk_bf16_f32 v53, v58, v59
	v_cvt_pk_bf16_f32 v54, v60, v61
	v_cvt_pk_bf16_f32 v55, v62, v63
	s_nop 0
	global_store_dwordx4 v22, v[48:51], s[72:73]
	global_store_dwordx4 v22, v[52:55], s[72:73] offset:16
	s_cbranch_vccnz .LBB0_1213
	s_andn2_b64 vcc, exec, s[10:11]
	s_cbranch_vccnz .LBB0_1212
	s_barrier
	s_branch .LBB0_1212

; __device__ __forceinline__ unsigned xb_ld(unsigned* p)              { return __hip_atomic_load(p, __ATOMIC_RELAXED, __HIP_MEMORY_SCOPE_AGENT); }
; __device__ __forceinline__ unsigned xb_add(unsigned* p, unsigned v) { return __hip_atomic_fetch_add(p, v, __ATOMIC_RELAXED, __HIP_MEMORY_SCOPE_AGENT); }
; #define XB_SPIN(cond, bar) do { unsigned _sp = 0; while (cond) { __builtin_amdgcn_s_sleep(1); \
;     if ((++_sp & 255u) == 0u) { if (xb_ld(&(bar)[XB_TMO])) break; if (_sp > XB_SPIN_CAP) { atomicAdd(&(bar)[XB_TMO], 1u); break; } } } } while (0)
; __device__ __forceinline__ void xcd_barrier(const XcdBarrier& b) {
;     ...
;         if (nloc == 0u) { xcd_barrier_complete(bar, b.x, nloc, nx); b.st[0] = nloc; b.st[1] = nx; }
;         const unsigned old = xb_add(&bar[XB_XSUB(b.x)], 1u);
;         const unsigned gen = old / nloc;
;         if (old + 1u == (gen + 1u) * nloc) {
;             __builtin_amdgcn_fence(__ATOMIC_RELEASE, "agent");
;             asm volatile("s_waitcnt vmcnt(0)" ::: "memory");
;             const unsigned og = xb_add(&bar[XB_TOP], 1u);
;             const unsigned tg = og / nx;
;             if (og + 1u == (tg + 1u) * nx) xb_add(&bar[XB_TOPGEN], 1u);
;             else XB_SPIN(xb_ld(&bar[XB_TOPGEN]) == tg, bar);
;             __builtin_amdgcn_fence(__ATOMIC_ACQUIRE, "agent");
;             xb_add(&bar[XB_XGEN(b.x)], 1u);
;             asm volatile("s_waitcnt vmcnt(0)" ::: "memory");
;         } else {
;             XB_SPIN(xb_ld(&bar[XB_XGEN(b.x)]) == gen, bar);
.LBB0_1665:
	s_lshl_b32 s2, s92, 8
	v_readlane_b32 s4, v255, 8
	v_readlane_b32 s5, v255, 9
	s_add_u32 s2, s4, s2
	s_addc_u32 s3, s5, 0
	v_mov_b32_e32 v1, 0x1000
	v_mov_b32_e32 v3, 1
	global_atomic_add v3, v1, v3, s[2:3] offset:1024 sc0
	v_cvt_f32_u32_e32 v1, v2
	v_sub_u32_e32 v4, 0, v2
	v_rcp_iflag_f32_e32 v1, v1
	s_nop 0
	v_mul_f32_e32 v1, 0x4f7ffffe, v1
	v_cvt_u32_f32_e32 v1, v1
	v_mul_lo_u32 v4, v4, v1
	v_mul_hi_u32 v4, v1, v4
	v_add_u32_e32 v1, v1, v4
	s_waitcnt vmcnt(0)
	v_mul_hi_u32 v1, v3, v1
	v_mul_lo_u32 v4, v1, v2
	v_sub_u32_e32 v4, v3, v4
	v_add_u32_e32 v5, 1, v1
	v_cmp_ge_u32_e32 vcc, v4, v2
	v_add_u32_e32 v3, 1, v3
	s_nop 0
	v_cndmask_b32_e32 v1, v1, v5, vcc
	v_sub_u32_e32 v5, v4, v2
	v_cndmask_b32_e32 v4, v4, v5, vcc
	v_add_u32_e32 v5, 1, v1
	v_cmp_ge_u32_e32 vcc, v4, v2
	s_nop 1
	v_cndmask_b32_e32 v1, v1, v5, vcc
	v_mul_lo_u32 v4, v2, v1
	v_add_u32_e32 v2, v4, v2
	v_cmp_ne_u32_e32 vcc, v3, v2
	s_and_saveexec_b64 s[4:5], vcc
	s_xor_b64 s[4:5], exec, s[4:5]
	s_cbranch_execz .LBB0_1679
	s_waitcnt lgkmcnt(0)
	v_readlane_b32 s8, v255, 8
	v_readlane_b32 s9, v255, 9
	v_mov_b32_e32 v0, 0
	s_nop 3
	s_add_u32 s8, s8, 0x3500
	s_addc_u32 s9, s9, 0
	global_load_dword v0, v0, s[8:9] sc1
	s_waitcnt vmcnt(0)
	v_cmp_eq_u32_e32 vcc, v0, v1
	s_and_saveexec_b64 s[6:7], vcc
	s_cbranch_execz .LBB0_1678
	s_mov_b32 s20, 1
	s_mov_b64 s[10:11], 0
	v_mov_b32_e32 v0, 0
	s_branch .LBB0_1669

; __device__ __forceinline__ unsigned xb_ld(unsigned* p)              { return __hip_atomic_load(p, __ATOMIC_RELAXED, __HIP_MEMORY_SCOPE_AGENT); }
; __device__ __forceinline__ unsigned xb_add(unsigned* p, unsigned v) { return __hip_atomic_fetch_add(p, v, __ATOMIC_RELAXED, __HIP_MEMORY_SCOPE_AGENT); }
; #define XB_SPIN(cond, bar) do { unsigned _sp = 0; while (cond) { __builtin_amdgcn_s_sleep(1); \
;     if ((++_sp & 255u) == 0u) { if (xb_ld(&(bar)[XB_TMO])) break; if (_sp > XB_SPIN_CAP) { atomicAdd(&(bar)[XB_TMO], 1u); break; } } } } while (0)
; __device__ __forceinline__ void xcd_barrier(const XcdBarrier& b) {
;     ...
;             const unsigned og = xb_add(&bar[XB_TOP], 1u);
;             const unsigned tg = og / nx;
;             if (og + 1u == (tg + 1u) * nx) xb_add(&bar[XB_TOPGEN], 1u);
;             else XB_SPIN(xb_ld(&bar[XB_TOPGEN]) == tg, bar);
;             __builtin_amdgcn_fence(__ATOMIC_ACQUIRE, "agent");
;             xb_add(&bar[XB_XGEN(b.x)], 1u);
;             asm volatile("s_waitcnt vmcnt(0)" ::: "memory");
.LBB0_1696:
	s_or_b64 exec, exec, s[4:5]
	v_mov_b32_e32 v0, 0x2000
	v_mov_b32_e32 v1, 1
	s_waitcnt vmcnt(0)
	buffer_inv sc1
	s_waitcnt vmcnt(0)
